# DN phase: 96 pool-GEMM workgroups run the expert-weight copies first (3 tiles after), 96 others take a sixth tile
# speedup vs baseline: 1.0097x; 1.0097x over previous
; #define LAS __attribute__((address_space(3)))
; __global__ void __launch_bounds__(NTHR, 2) fwd(Args args) {
;     extern __shared__ __attribute__((aligned(16))) unsigned char lds_raw[];
;     Frame F;
;     F.lds = (LAS unsigned char*)lds_raw; F.MISC = (volatile LAS unsigned*)(F.lds + MISC_OFF);
;     F.tid = threadIdx.x; F.lane = F.tid & 63; F.wave = __builtin_amdgcn_readfirstlane(F.tid >> 6);
;     F.G = gridDim.x; { const int bx = blockIdx.x; F.vcu = (F.G % 8 == 0) ? (bx % 8) * (F.G / 8) + bx / 8 : bx; }
;     F.ws = args.ws; F.ctl = (unsigned*)(args.ws + WS_CTL); F.out = args.out;
_Z3fwd4Args:
	s_mov_b32 s98, 0
	s_load_dword s31, s[0:1], 0xe8
	s_mov_b64 s[24:25], s[0:1]
	s_add_u32 s0, s24, 0xe8
	s_addc_u32 s1, s25, 0
	v_readfirstlane_b32 s97, v0
	v_writelane_b32 v247, s0, 0
	s_mov_b32 s96, s2
	s_nop 0
	v_writelane_b32 v247, s1, 1
	s_waitcnt lgkmcnt(0)
	s_and_b32 s0, s31, 7
	s_cmp_lg_u32 s0, 0
	s_mov_b32 s0, s2
	v_writelane_b32 v247, s0, 2
	s_nop 1
	v_writelane_b32 v247, s1, 3
	s_cbranch_scc1 .LBB0_2
	v_readlane_b32 s2, v247, 2
	s_ashr_i32 s1, s2, 31
	s_lshr_b32 s1, s1, 29
	s_add_i32 s1, s2, s1
	s_mov_b32 s4, s2
	s_and_b32 s2, s1, -8
	s_ashr_i32 s0, s31, 3
	s_sub_i32 s2, s4, s2
	s_mul_i32 s0, s0, s2
	s_ashr_i32 s1, s1, 3
	s_add_i32 s96, s0, s1
	v_readlane_b32 s3, v247, 3

; __global__ void __launch_bounds__(NTHR, 2) fwd(Args args) {
;     ...
;         } } else if (!(args.flags & 2)) {
;             pg8::DenseOrder S; S.init(T, D, D_POOL, F.G - NB * NH, (int)blockIdx.x - NB * NH); EpiPool E{GP, MP};
;             if (!(args.flags & 8)) pg8::gemm_phase<EpiPool, pg8::DenseOrder, false, true, true, true>(F.lds + RING_OFF, DBUF, WCOMB, D_POOL, S, E);
;         }
;         if (!(args.flags & 4)) {
.LBB0_928:
	v_readlane_b32 s6, v247, 45
	v_readlane_b32 s7, v247, 46
	s_load_dwordx2 s[4:5], s[6:7], 0xd8
	s_load_dwordx4 s[8:11], s[6:7], 0xc0
	s_waitcnt lgkmcnt(0)
	s_cmp_lt_i32 s4, 5
	s_cselect_b64 s[4:5], -1, 0
	s_add_u32 s66, s2, 0x3f00000
	s_addc_u32 s67, s3, 0
	s_add_u32 s68, s2, 0xbf00000
	s_addc_u32 s69, s3, 0
	s_add_u32 s64, s10, 0xc000000
	s_addc_u32 s65, s11, 0
	s_add_u32 s70, s2, 0x23f00000
	s_addc_u32 s71, s3, 0
	s_and_b64 s[4:5], s[4:5], s[0:1]
	s_andn2_b64 vcc, exec, s[4:5]
	s_cbranch_vccnz .LBB0_1014
	s_load_dword s33, s[6:7], 0xe0
	v_readlane_b32 s0, v247, 2
	v_readlane_b32 s1, v247, 3
	s_cmp_gt_i32 s0, 31
	s_mov_b64 s[0:1], -1
	s_cbranch_scc0 .LBB0_971
	s_waitcnt lgkmcnt(0)
	s_bitcmp1_b32 s33, 1
	s_cbranch_scc1 .LBB0_970
	s_bitcmp1_b32 s33, 3
	s_cbranch_scc1 .LBB0_970
	s_cmp_lg_u32 s98, 0
	s_cbranch_scc1 .Lpool_go
	v_readlane_b32 s99, v247, 2
	s_nop 3
	s_cmp_lt_u32 s99, 160
	s_cbranch_scc1 .Lpool_go
	s_mov_b32 s98, 1
	v_writelane_b32 v248, s0, 0
	v_writelane_b32 v248, s1, 1
	v_writelane_b32 v248, s2, 2
	v_writelane_b32 v248, s3, 3
	v_writelane_b32 v248, s4, 4
	v_writelane_b32 v248, s5, 5
	v_writelane_b32 v248, s6, 6
	v_writelane_b32 v248, s7, 7
	v_writelane_b32 v248, s8, 8
	v_writelane_b32 v248, s9, 9
	v_writelane_b32 v248, s10, 10
	v_writelane_b32 v248, s11, 11
	v_writelane_b32 v248, s12, 12
	v_writelane_b32 v248, s13, 13
	v_writelane_b32 v248, s14, 14
	v_writelane_b32 v248, s15, 15
	v_writelane_b32 v248, s16, 16
	v_writelane_b32 v248, s17, 17
	v_writelane_b32 v248, s18, 18
	v_writelane_b32 v248, s19, 19
	v_writelane_b32 v248, s20, 20
	v_writelane_b32 v248, s21, 21
	v_writelane_b32 v248, s22, 22
	v_writelane_b32 v248, s23, 23
	v_writelane_b32 v248, s24, 24
	v_writelane_b32 v248, s25, 25
	v_writelane_b32 v248, s26, 26
	v_writelane_b32 v248, s27, 27
	v_writelane_b32 v248, s28, 28
	v_writelane_b32 v248, s29, 29
	v_writelane_b32 v248, s30, 30
	v_writelane_b32 v248, s31, 31
	v_writelane_b32 v248, s32, 32
	v_writelane_b32 v248, s33, 33
	v_writelane_b32 v248, s34, 34
	v_writelane_b32 v248, s35, 35
	v_writelane_b32 v248, s36, 36
	v_writelane_b32 v248, s37, 37
	v_writelane_b32 v248, s38, 38
	v_writelane_b32 v248, s39, 39
	v_writelane_b32 v248, s40, 40
	v_writelane_b32 v248, s41, 41
	v_writelane_b32 v248, s42, 42
	v_writelane_b32 v248, s43, 43
	v_writelane_b32 v248, s44, 44
	v_writelane_b32 v248, s45, 45
	v_writelane_b32 v248, s46, 46
	v_writelane_b32 v248, s47, 47
	v_writelane_b32 v248, s48, 48
	v_writelane_b32 v248, s49, 49
	v_writelane_b32 v248, s50, 50
	v_writelane_b32 v248, s51, 51
	v_writelane_b32 v248, s52, 52
	v_writelane_b32 v248, s53, 53
	v_writelane_b32 v248, s54, 54
	v_writelane_b32 v248, s55, 55
	v_writelane_b32 v248, s56, 56
	v_writelane_b32 v248, s57, 57
	v_writelane_b32 v248, s58, 58
	v_writelane_b32 v248, s59, 59
	v_writelane_b32 v248, s60, 60
	v_writelane_b32 v248, s61, 61
	v_writelane_b32 v248, s62, 62
	v_writelane_b32 v248, s63, 63
	v_writelane_b32 v249, s64, 0
	v_writelane_b32 v249, s65, 1
	v_writelane_b32 v249, s66, 2
	v_writelane_b32 v249, s67, 3
	v_writelane_b32 v249, s68, 4
	v_writelane_b32 v249, s69, 5
	v_writelane_b32 v249, s70, 6
	v_writelane_b32 v249, s71, 7
	v_writelane_b32 v249, s72, 8
	v_writelane_b32 v249, s73, 9
	v_writelane_b32 v249, s74, 10
	v_writelane_b32 v249, s75, 11
	v_writelane_b32 v249, s76, 12
	v_writelane_b32 v249, s77, 13
	v_writelane_b32 v249, s78, 14
	v_writelane_b32 v249, s79, 15
	v_writelane_b32 v249, s80, 16
	v_writelane_b32 v249, s81, 17
	v_writelane_b32 v249, s82, 18
	v_writelane_b32 v249, s83, 19
	v_writelane_b32 v249, s84, 20
	v_writelane_b32 v249, s85, 21
	v_writelane_b32 v249, s86, 22
	v_writelane_b32 v249, s87, 23
	v_writelane_b32 v249, s88, 24
	v_writelane_b32 v249, s89, 25
	v_writelane_b32 v249, s90, 26
	v_writelane_b32 v249, s91, 27
	v_writelane_b32 v249, s92, 28
	v_writelane_b32 v249, s93, 29
	v_writelane_b32 v249, s94, 30
	v_writelane_b32 v249, s95, 31
	v_writelane_b32 v249, s96, 32
	v_writelane_b32 v249, s97, 33
	v_writelane_b32 v249, vcc_lo, 40
	v_writelane_b32 v249, vcc_hi, 41
	v_mov_b32_e32 v250, v246
	v_mov_b32_e32 v251, v247
	v_mov_b32_e32 v252, v0
	v_mov_b32_e32 v253, v1
	s_branch .LBB0_998
.Lpool_go:
	v_readlane_b32 s0, v247, 2
	s_sub_i32 s62, s0, 32
	v_readlane_b32 s1, v247, 3
	s_cmpk_lt_u32 s62, 0x400
	s_cselect_b64 s[0:1], -1, 0
	s_cmpk_gt_u32 s62, 0x3ff
	v_readfirstlane_b32 s8, v0
	s_cbranch_scc1 .LBB0_934
	v_readlane_b32 s6, v247, 2
	v_readlane_b32 s7, v247, 3
	s_lshl_b32 s6, s6, 7
	s_lshr_b32 s7, s62, 3
	s_or_b32 s6, s6, s7
	s_lshr_b32 s6, s6, 3
	s_and_b32 s6, s6, 0x78
	s_bfe_u32 s7, s62, 0x30003
	s_or_b32 s6, s6, s7
	s_bfe_u32 s52, s62, 0x30006
	s_lshl_b32 s10, s6, 8

;     __device__ __forceinline__ bool next(int i, Unit& u) const {
;         const long L = (long)i * G + c; if (L >= nwg) return false;
;         unit_of((int)L, u); return true;
; template <class Epi, class Sched, bool GATHER, bool ALIGN_EPI = true, bool SP2 = true, bool REMAP64 = false>
; __device__ __forceinline__ void gemm_phase(LAS unsigned char* lds, const bf16* Ag, const bf16* Btg, const int K, const Sched& S, const Epi& E) {
;     ...
;         const bool has_next = S.next(ui + 1, nxt);
.LBB0_940:
	s_add_i32 s75, s75, 1
	s_mul_i32 s8, s75, s87
	s_mul_hi_u32 s9, s75, s77
	s_add_i32 s9, s9, s8
	s_mul_i32 s8, s75, s77
	s_add_u32 s26, s8, s62
	s_addc_u32 s27, s9, 0
	s_cmp_lt_u32 s62, 128
	s_cbranch_scc1 .Lpool_y
	s_cmp_ge_u32 s75, 3
	s_cbranch_scc0 .Lpool_sched_done
	s_movk_i32 s26, 0x7fff
	s_mov_b32 s27, 0
	s_branch .Lpool_sched_done
.Lpool_y:
	s_cmp_eq_u32 s75, 5
	s_cbranch_scc0 .Lpool_sched_done
	s_cmp_lt_u32 s62, 96
	s_cbranch_scc0 .Lpool_sched_done
	s_add_u32 s26, s62, 800
	s_mov_b32 s27, 0
.Lpool_sched_done:
	v_cmp_gt_i64_e32 vcc, s[26:27], v[166:167]
	v_cmp_lt_i64_e64 s[8:9], s[26:27], v[164:165]
	s_cbranch_vccnz .LBB0_946
	s_ashr_i32 s11, s26, 31
	s_lshr_b32 s11, s11, 29
	s_add_i32 s11, s26, s11
	s_and_b32 s22, s11, -8
	s_sub_i32 s24, s26, s22
	s_cmp_gt_i32 s24, -1
	s_mov_b64 s[22:23], -1
	s_cbranch_scc0 .LBB0_943
	s_lshl_b32 s25, s24, 7
	s_mov_b64 s[22:23], 0

; __global__ void __launch_bounds__(NTHR, 2) fwd(Args args) {
;     ...
;         if (!(args.flags & 4)) {
;             constexpr int IT_GU = NE * (D / 128) * 32, PER_DN = (DE / 128) * (D / 32), IT_ALL = IT_GU + NE * PER_DN;
;             for (;;) {
;                 int it0 = 0; if (lane == 0) it0 = (int)atomicAdd(&F.ctl[CW_TR], 4u);
;                 it0 = __builtin_amdgcn_readfirstlane(it0);
;                 if (it0 >= IT_ALL) break;
; #pragma unroll 1
;                 for (int it = it0; it < it0 + 4; ++it) {
;                     if (it < IT_GU) {
;                         const int e = it / (16 * 32), rem = it % (16 * 32), kb = rem / 32, nb = rem % 32;
;                         const int r0 = 32 * nb, pn = r0 >> 8, rin = r0 & 255; const bool up = rin >= 128; const int c0 = pn * 128 + (rin & 127);
;                         transpose_item((up ? F.in[I_W_UP] : F.in[I_W_GATE]) + (size_t)e * D * DE, DE, D, 128 * kb, c0, 32, WGU + (size_t)e * 1024 * D, r0, nullptr, lane);
;                     } else {
;                         const int j = it - IT_GU, e = j / PER_DN, rem = j % PER_DN, kb = rem / (D / 32), nb = rem % (D / 32);
;                         transpose_item(F.in[I_W_DOWN] + (size_t)e * DE * D, D, DE, 128 * kb, 32 * nb, 32, WDN + (size_t)e * D * DE, 32 * nb, nullptr, lane);
;                     }
;                 }
;             }
;         }
;         __syncthreads();
.LBB0_1013:
	s_cmp_eq_u32 s98, 1
	s_cbranch_scc0 .Lpool_fin
	s_mov_b32 s98, 2
	v_readlane_b32 s0, v248, 0
	v_readlane_b32 s1, v248, 1
	v_readlane_b32 s2, v248, 2
	v_readlane_b32 s3, v248, 3
	v_readlane_b32 s4, v248, 4
	v_readlane_b32 s5, v248, 5
	v_readlane_b32 s6, v248, 6
	v_readlane_b32 s7, v248, 7
	v_readlane_b32 s8, v248, 8
	v_readlane_b32 s9, v248, 9
	v_readlane_b32 s10, v248, 10
	v_readlane_b32 s11, v248, 11
	v_readlane_b32 s12, v248, 12
	v_readlane_b32 s13, v248, 13
	v_readlane_b32 s14, v248, 14
	v_readlane_b32 s15, v248, 15
	v_readlane_b32 s16, v248, 16
	v_readlane_b32 s17, v248, 17
	v_readlane_b32 s18, v248, 18
	v_readlane_b32 s19, v248, 19
	v_readlane_b32 s20, v248, 20
	v_readlane_b32 s21, v248, 21
	v_readlane_b32 s22, v248, 22
	v_readlane_b32 s23, v248, 23
	v_readlane_b32 s24, v248, 24
	v_readlane_b32 s25, v248, 25
	v_readlane_b32 s26, v248, 26
	v_readlane_b32 s27, v248, 27
	v_readlane_b32 s28, v248, 28
	v_readlane_b32 s29, v248, 29
	v_readlane_b32 s30, v248, 30
	v_readlane_b32 s31, v248, 31
	v_readlane_b32 s32, v248, 32
	v_readlane_b32 s33, v248, 33
	v_readlane_b32 s34, v248, 34
	v_readlane_b32 s35, v248, 35
	v_readlane_b32 s36, v248, 36
	v_readlane_b32 s37, v248, 37
	v_readlane_b32 s38, v248, 38
	v_readlane_b32 s39, v248, 39
	v_readlane_b32 s40, v248, 40
	v_readlane_b32 s41, v248, 41
	v_readlane_b32 s42, v248, 42
	v_readlane_b32 s43, v248, 43
	v_readlane_b32 s44, v248, 44
	v_readlane_b32 s45, v248, 45
	v_readlane_b32 s46, v248, 46
	v_readlane_b32 s47, v248, 47
	v_readlane_b32 s48, v248, 48
	v_readlane_b32 s49, v248, 49
	v_readlane_b32 s50, v248, 50
	v_readlane_b32 s51, v248, 51
	v_readlane_b32 s52, v248, 52
	v_readlane_b32 s53, v248, 53
	v_readlane_b32 s54, v248, 54
	v_readlane_b32 s55, v248, 55
	v_readlane_b32 s56, v248, 56
	v_readlane_b32 s57, v248, 57
	v_readlane_b32 s58, v248, 58
	v_readlane_b32 s59, v248, 59
	v_readlane_b32 s60, v248, 60
	v_readlane_b32 s61, v248, 61
	v_readlane_b32 s62, v248, 62
	v_readlane_b32 s63, v248, 63
	v_readlane_b32 s64, v249, 0
	v_readlane_b32 s65, v249, 1
	v_readlane_b32 s66, v249, 2
	v_readlane_b32 s67, v249, 3
	v_readlane_b32 s68, v249, 4
	v_readlane_b32 s69, v249, 5
	v_readlane_b32 s70, v249, 6
	v_readlane_b32 s71, v249, 7
	v_readlane_b32 s72, v249, 8
	v_readlane_b32 s73, v249, 9
	v_readlane_b32 s74, v249, 10
	v_readlane_b32 s75, v249, 11
	v_readlane_b32 s76, v249, 12
	v_readlane_b32 s77, v249, 13
	v_readlane_b32 s78, v249, 14
	v_readlane_b32 s79, v249, 15
	v_readlane_b32 s80, v249, 16
	v_readlane_b32 s81, v249, 17
	v_readlane_b32 s82, v249, 18
	v_readlane_b32 s83, v249, 19
	v_readlane_b32 s84, v249, 20
	v_readlane_b32 s85, v249, 21
	v_readlane_b32 s86, v249, 22
	v_readlane_b32 s87, v249, 23
	v_readlane_b32 s88, v249, 24
	v_readlane_b32 s89, v249, 25
	v_readlane_b32 s90, v249, 26
	v_readlane_b32 s91, v249, 27
	v_readlane_b32 s92, v249, 28
	v_readlane_b32 s93, v249, 29
	v_readlane_b32 s94, v249, 30
	v_readlane_b32 s95, v249, 31
	v_readlane_b32 s96, v249, 32
	v_readlane_b32 s97, v249, 33
	v_readlane_b32 vcc_lo, v249, 40
	v_readlane_b32 vcc_hi, v249, 41
	v_mov_b32_e32 v246, v250
	v_mov_b32_e32 v247, v251
	v_mov_b32_e32 v0, v252
	v_mov_b32_e32 v1, v253
	s_nop 7
	s_branch .Lpool_go

; __global__ void __launch_bounds__(NTHR, 2) fwd(Args args) {
;     extern __shared__ __attribute__((aligned(16))) unsigned char lds_raw[];
	.amdhsa_kernel _Z3fwd4Args
		.amdhsa_group_segment_fixed_size 0
		.amdhsa_private_segment_fixed_size 0
		.amdhsa_kernarg_size 488
		.amdhsa_user_sgpr_count 2
		.amdhsa_user_sgpr_dispatch_ptr 0
		.amdhsa_user_sgpr_queue_ptr 0
		.amdhsa_user_sgpr_kernarg_segment_ptr 1
		.amdhsa_user_sgpr_dispatch_id 0
		.amdhsa_user_sgpr_kernarg_preload_length 0
		.amdhsa_user_sgpr_kernarg_preload_offset 0
		.amdhsa_user_sgpr_private_segment_size 0
		.amdhsa_uses_dynamic_stack 0
		.amdhsa_enable_private_segment 0
		.amdhsa_system_sgpr_workgroup_id_x 1
		.amdhsa_system_sgpr_workgroup_id_y 0
		.amdhsa_system_sgpr_workgroup_id_z 0
		.amdhsa_system_sgpr_workgroup_info 0
		.amdhsa_system_vgpr_workitem_id 0
		.amdhsa_next_free_vgpr 256
		.amdhsa_next_free_sgpr 100
		.amdhsa_accum_offset 256
		.amdhsa_reserve_vcc 1
		.amdhsa_float_round_mode_32 0
		.amdhsa_float_round_mode_16_64 0
		.amdhsa_float_denorm_mode_32 3
		.amdhsa_float_denorm_mode_16_64 3
		.amdhsa_dx10_clamp 1
		.amdhsa_ieee_mode 1
		.amdhsa_fp16_overflow 0
		.amdhsa_tg_split 0
		.amdhsa_exception_fp_ieee_invalid_op 0
		.amdhsa_exception_fp_denorm_src 0
		.amdhsa_exception_fp_ieee_div_zero 0
		.amdhsa_exception_fp_ieee_overflow 0
		.amdhsa_exception_fp_ieee_underflow 0
		.amdhsa_exception_fp_ieee_inexact 0
		.amdhsa_exception_int_div_zero 0
	.end_amdhsa_kernel

; __global__ void __launch_bounds__(NTHR, 2) fwd(Args args) {
;     extern __shared__ __attribute__((aligned(16))) unsigned char lds_raw[];
amdhsa.kernels:
  - .agpr_count:     0
    .args:
      - .offset:         0
        .size:           232
        .value_kind:     by_value
      - .offset:         232
        .size:           4
        .value_kind:     hidden_block_count_x
      - .offset:         236
        .size:           4
        .value_kind:     hidden_block_count_y
      - .offset:         240
        .size:           4
        .value_kind:     hidden_block_count_z
      - .offset:         244
        .size:           2
        .value_kind:     hidden_group_size_x
      - .offset:         246
        .size:           2
        .value_kind:     hidden_group_size_y
      - .offset:         248
        .size:           2
        .value_kind:     hidden_group_size_z
      - .offset:         250
        .size:           2
        .value_kind:     hidden_remainder_x
      - .offset:         252
        .size:           2
        .value_kind:     hidden_remainder_y
      - .offset:         254
        .size:           2
        .value_kind:     hidden_remainder_z
      - .offset:         272
        .size:           8
        .value_kind:     hidden_global_offset_x
      - .offset:         280
        .size:           8
        .value_kind:     hidden_global_offset_y
      - .offset:         288
        .size:           8
        .value_kind:     hidden_global_offset_z
      - .offset:         296
        .size:           2
        .value_kind:     hidden_grid_dims
      - .offset:         352
        .size:           4
        .value_kind:     hidden_dynamic_lds_size
    .group_segment_fixed_size: 0
    .kernarg_segment_align: 8
    .kernarg_segment_size: 488
    .language:       OpenCL C
    .language_version:
      - 2
      - 0
    .max_flat_workgroup_size: 512
    .name:           _Z3fwd4Args
    .private_segment_fixed_size: 0
    .sgpr_count:     106
    .sgpr_spill_count: 113
    .symbol:         _Z3fwd4Args.kd
    .uniform_work_group_size: 1
    .uses_dynamic_stack: false
    .vgpr_count:     256
    .vgpr_spill_count: 0
    .wavefront_size: 64
